# GDN chain loader prologue: three stages loaded back to back, first fill waits for stage one only
# baseline (speedup 1.0000x reference)
; __device__ void phase_gdn_chain(const Params& p, int l, char* smem, int vb, int nvb, int oz) {
;     ...
;             GDN_LOAD(ra, va, ga, 0)
;             GDN_LOAD(rb, vb_, gb, 1)
;             GDN_LOAD(rc, vc_, gc, 2)
.LBB0_418:
	s_or_saveexec_b64 s[0:1], s[48:49]
	v_readlane_b32 s14, v254, 11
	v_readlane_b32 s4, v254, 1
	v_readlane_b32 s5, v254, 2
	v_readlane_b32 s6, v254, 3
	v_readlane_b32 s7, v254, 4
	v_readlane_b32 s8, v254, 5
	v_readlane_b32 s9, v254, 6
	v_readlane_b32 s10, v254, 7
	v_readlane_b32 s11, v254, 8
	v_readlane_b32 s12, v254, 9
	v_readlane_b32 s13, v254, 10
	v_readlane_b32 s15, v254, 12
	s_xor_b64 exec, exec, s[0:1]
	s_cbranch_execz .LBB0_389
	s_lshl_b32 s3, s46, 2
	s_or_b32 s2, s3, s2
	s_mul_i32 s2, s2, 36
	s_or_b32 s24, s2, s82
	s_ashr_i32 s25, s24, 31
	s_add_u32 s26, s24, s84
	s_addc_u32 s27, s25, 0
	s_lshl_b64 s[42:43], s[26:27], 13
	s_add_u32 s46, s4, s42
	s_addc_u32 s47, s5, s43
	s_add_u32 s48, s6, s42
	s_addc_u32 s49, s7, s43
	s_lshl_b64 s[24:25], s[24:25], 13
	s_add_u32 s50, s8, s24
	s_addc_u32 s51, s9, s25
	s_add_u32 s24, s10, s24
	s_addc_u32 s25, s11, s25
	s_add_u32 s42, s12, s42
	v_lshlrev_b32_e32 v2, 1, v202
	s_addc_u32 s43, s13, s43
	v_lshlrev_b32_e32 v215, 1, v204
	global_load_dwordx4 v[148:151], v2, s[46:47]
	global_load_dwordx4 v[152:155], v2, s[48:49]
	global_load_dwordx4 v[156:159], v215, s[48:49]
	global_load_dwordx4 v[160:163], v215, s[50:51]
	global_load_dwordx4 v[168:171], v2, s[50:51]
	global_load_dwordx4 v[164:167], v2, s[24:25]
	global_load_dwordx4 v[184:187], v215, s[46:47]
	global_load_dwordx4 v[172:175], v2, s[42:43]
	global_load_dwordx4 v[180:183], v215, s[24:25]
	global_load_dwordx4 v[176:179], v215, s[42:43]
	s_lshl_b64 s[24:25], s[26:27], 10
	s_add_u32 s42, s14, s24
	s_addc_u32 s43, s15, s25
	v_mov_b32_e32 v217, 0
	v_lshlrev_b32_e32 v216, 2, v190
	v_mov_b32_e32 v218, 0
	s_and_saveexec_b64 s[46:47], s[38:39]
	s_cbranch_execz .LBB0_421
	global_load_dword v218, v216, s[42:43]

; __device__ void phase_gdn_chain(const Params& p, int l, char* smem, int vb, int nvb, int oz) {
;     ...
;             GDN_LOAD(ra, va, ga, 0)
;             GDN_LOAD(rb, vb_, gb, 1)
;             GDN_LOAD(rc, vc_, gc, 2)
;             GDN_FILL(ra, va, ga, 0)
;             GDN_LOAD(ra, va, ga, 3)
.LBB0_431:
	s_or_b64 exec, exec, s[46:47]
	v_add_u32_e32 v223, 0, v211
	s_waitcnt vmcnt(20)
	ds_write_b128 v223, v[148:151]
	ds_write_b128 v223, v[184:187] offset:4608
	ds_write_b128 v223, v[152:155] offset:9216
	ds_write_b128 v223, v[156:159] offset:13824
	ds_write_b128 v223, v[168:171] offset:18432
	ds_write_b128 v223, v[160:163] offset:23040
	ds_write_b128 v223, v[164:167] offset:27648
	ds_write_b128 v223, v[180:183] offset:32256
	ds_write_b128 v193, v[172:175] offset:36864
	ds_write_b128 v193, v[176:179] offset:40960
	s_and_saveexec_b64 s[42:43], s[38:39]
	ds_write_b32 v213, v218 offset:45056
	s_or_b64 exec, exec, s[42:43]
	s_and_saveexec_b64 s[42:43], s[40:41]
	ds_write_b32 v3, v217 offset:45568
	s_or_b64 exec, exec, s[42:43]
	s_or_b32 s24, s2, s85
	s_ashr_i32 s25, s24, 31
	s_add_u32 s26, s24, s84
	s_addc_u32 s27, s25, 0
	s_lshl_b64 s[42:43], s[26:27], 13
	s_add_u32 s46, s4, s42
	s_addc_u32 s47, s5, s43
	s_add_u32 s48, s6, s42
	s_addc_u32 s49, s7, s43
	s_lshl_b64 s[24:25], s[24:25], 13
	s_add_u32 s50, s8, s24
	s_addc_u32 s51, s9, s25
	s_add_u32 s24, s10, s24
	s_addc_u32 s25, s11, s25
	s_add_u32 s42, s12, s42
	s_addc_u32 s43, s13, s43
	global_load_dwordx4 v[148:151], v2, s[46:47]
	global_load_dwordx4 v[152:155], v2, s[48:49]
	global_load_dwordx4 v[156:159], v215, s[48:49]
	global_load_dwordx4 v[160:163], v215, s[50:51]
	global_load_dwordx4 v[164:167], v2, s[50:51]
	global_load_dwordx4 v[168:171], v2, s[24:25]
	global_load_dwordx4 v[172:175], v215, s[46:47]
	global_load_dwordx4 v[176:179], v2, s[42:43]
	global_load_dwordx4 v[180:183], v215, s[24:25]
	global_load_dwordx4 v[184:187], v215, s[42:43]
	s_lshl_b64 s[24:25], s[26:27], 10
	s_add_u32 s42, s14, s24
	s_addc_u32 s43, s15, s25
	s_and_saveexec_b64 s[46:47], s[38:39]
	s_cbranch_execz .LBB0_437
	global_load_dword v218, v216, s[42:43]
